# down GEMM walks each XCD's tile range in reverse (most recently written activations first)
# speedup vs baseline: 1.0016x; 1.0016x over previous
;     __device__ __forceinline__ bool next(int i, pg8::Unit& u) const {
;         const int L = i * G + c; const int xg = L % pg8::NXCD, off = L / pg8::NXCD;
;         const int tq = ntile / pg8::NXCD, tr = ntile % pg8::NXCD;
;         const int tcnt = tq + (xg < tr ? 1 : 0), tstart = xg * tq + (xg < tr ? xg : tr);
;         if (off >= tcnt * npn) return false;
;         const int tile = tstart + off / npn, pn = off % npn;
;         const int lane = lane_;
;         const bool hit = (tile >= ts[lane]) && (tile < ts[lane + 1]);
;         const unsigned long long mk = __ballot(hit);
;         const int e = mk ? (int)__builtin_ctzll(mk) : 64;
;         u.pm = tile; u.pn = pn;
;         u.bptr = (e < 64 ? Bexp + (size_t)e * bstride : Bsh) + (size_t)pn * 256 * ldb;
;         u.roff = -(tile * 256) - 1; u.nvalid = 256;
.LBB0_1691:
	v_readlane_b32 s2, v254, 46
	s_waitcnt lgkmcnt(0)
	s_barrier
	v_mov_b32_e32 v1, s2
	ds_read_b32 v1, v1
	s_ashr_i32 s51, s5, 6
	v_readfirstlane_b32 s48, v251
	s_mov_b32 s5, 2
	s_waitcnt lgkmcnt(0)
	v_readfirstlane_b32 s2, v1
	s_ashr_i32 s3, s2, 31
	s_lshr_b32 s3, s3, 29
	s_add_i32 s3, s2, s3
	s_ashr_i32 s6, s3, 3
	s_and_b32 s3, s3, -8
	s_sub_i32 s7, s2, s3
	s_cmp_lt_i32 s78, s7
	s_cselect_b64 s[2:3], -1, 0
	s_cmp_lg_u64 s[2:3], 0
	s_addc_u32 s2, s6, 0
	s_lshl_b32 s2, s2, 2
	v_readlane_b32 s3, v254, 3
	s_cmp_ge_i32 s3, s2
	s_cbranch_scc1 .LBB0_1718
	v_lshl_add_u32 v0, v0, 2, 0
	v_add_u32_e32 v214, 0x21080, v0
	ds_read_b32 v0, v214
	s_min_i32 s3, s78, s7
	v_readlane_b32 s8, v253, 52
	s_mul_i32 s2, s6, s78
	s_add_i32 s83, s3, s2
	s_cmp_lt_i32 s78, s7
	s_addc_u32 s3, s6, 0
	s_add_i32 s83, s83, s3
	s_sub_i32 s83, s83, s8
	s_add_i32 s83, s83, -1
	s_waitcnt lgkmcnt(0)
	v_cmp_ge_i32_e32 vcc, s83, v0
	s_mov_b64 s[42:43], 0
	s_and_saveexec_b64 s[2:3], vcc
	s_cbranch_execz .LBB0_1694
	ds_read_b32 v0, v214 offset:4
	s_waitcnt lgkmcnt(0)
	v_cmp_lt_i32_e32 vcc, s83, v0
	s_and_b64 s[42:43], vcc, exec

;     __device__ __forceinline__ bool next(int i, pg8::Unit& u) const {
;         const int L = i * G + c; const int xg = L % pg8::NXCD, off = L / pg8::NXCD;
;         const int tq = ntile / pg8::NXCD, tr = ntile % pg8::NXCD;
;         const int tcnt = tq + (xg < tr ? 1 : 0), tstart = xg * tq + (xg < tr ? xg : tr);
;         if (off >= tcnt * npn) return false;
;         const int tile = tstart + off / npn, pn = off % npn;
;         const int lane = lane_;
;         const bool hit = (tile >= ts[lane]) && (tile < ts[lane + 1]);
;         const unsigned long long mk = __ballot(hit);
;         const int e = mk ? (int)__builtin_ctzll(mk) : 64;
;         u.pm = tile; u.pn = pn;
;         u.bptr = (e < 64 ? Bexp + (size_t)e * bstride : Bsh) + (size_t)pn * 256 * ldb;
;         u.roff = -(tile * 256) - 1; u.nvalid = 256;
.LBB0_1699:
	s_add_i32 s77, s77, 1
	s_mul_i32 s40, s77, s33
	v_readlane_b32 s41, v252, 10
	s_add_i32 s40, s40, s41
	s_ashr_i32 s41, s40, 31
	s_lshr_b32 s54, s41, 29
	s_add_i32 s54, s40, s54
	s_ashr_i32 s60, s54, 3
	s_and_b32 s54, s54, -8
	s_sub_i32 s61, s40, s54
	s_cmp_lt_i32 s61, s7
	s_cselect_b64 s[54:55], -1, 0
	s_cmp_lg_u64 s[54:55], 0
	s_addc_u32 s54, s6, 0
	s_lshl_b32 s62, s54, 2
	s_cmp_lt_i32 s60, s62
	s_cselect_b64 s[54:55], -1, 0
	s_cmp_ge_i32 s60, s62
	s_cbranch_scc1 .LBB0_1703
	s_lshr_b32 s41, s41, 27
	ds_read_b32 v4, v214
	s_add_i32 s40, s40, s41
	s_min_i32 s51, s61, s7
	s_ashr_i32 s40, s40, 5
	s_mul_i32 s50, s61, s6
	s_lshr_b32 s41, s62, 2
	s_sub_i32 s40, s41, s40
	s_add_i32 s40, s40, s51
	s_add_i32 s40, s40, s50
	s_add_i32 s82, s40, -1
	s_waitcnt lgkmcnt(0)
	v_cmp_ge_i32_e32 vcc, s82, v4
	s_mov_b64 s[40:41], 0
	s_and_saveexec_b64 s[50:51], vcc
	s_cbranch_execz .LBB0_1702
	ds_read_b32 v4, v214 offset:4
	s_waitcnt lgkmcnt(0)
	v_cmp_lt_i32_e32 vcc, s82, v4
	s_and_b64 s[40:41], vcc, exec
